# P14 unit epilogues un-aligned (template's ALIGN_EPI=false form): leading half starts its epilogue beside the trailing half's last MFMA block; offset undone once at phase end
# baseline (speedup 1.0000x reference)
.LBB0_1084:
	ds_read_b128 v[164:167], v152
	ds_read_b128 v[168:171], v152 offset:1024
	ds_read_b128 v[172:175], v152 offset:2048
	ds_read_b128 v[176:179], v152 offset:3072
	ds_read_b128 v[180:183], v153
	ds_read_b128 v[184:187], v153 offset:1024
	ds_read_b128 v[224:227], v153 offset:2048
	ds_read_b128 v[228:231], v153 offset:3072
	s_add_u32 s30, s26, 0xfffc0080
	s_addc_u32 s31, s27, -1
	s_cmp_eq_u32 s63, 12
	s_cselect_b32 s35, s17, s31
	s_cselect_b32 s34, s59, s30
	s_cselect_b32 s31, s19, s62
	s_cselect_b32 s30, s60, s61
	v_lshl_add_u64 v[148:149], s[26:27], 0, v[142:143]
	s_add_i32 m0, s25, 0xc000
	ds_read_b128 v[192:195], v154
	ds_read_b128 v[196:199], v154 offset:1024
	ds_read_b128 v[200:203], v154 offset:2048
	ds_read_b128 v[204:207], v154 offset:3072
	ds_read_b128 v[208:211], v154 offset:4096
	ds_read_b128 v[212:215], v154 offset:5120
	ds_read_b128 v[216:219], v154 offset:6144
	ds_read_b128 v[220:223], v154 offset:7168
	global_load_lds_dwordx4 v[148:149], off
	v_lshl_add_u64 v[148:149], s[26:27], 0, v[144:145]
	s_add_i32 m0, s25, 0xe000
	s_nop 0
	global_load_lds_dwordx4 v[148:149], off
	s_waitcnt vmcnt(8)
	s_waitcnt lgkmcnt(0)
	s_barrier
	s_setprio 1
	s_waitcnt lgkmcnt(0)
	s_nop 0
	v_mfma_scale_f32_16x16x128_f8f6f4 v[126:129], v[164:171], v[192:199], v[126:129], v156, v155 op_sel_hi:[0,0,0]
	v_mfma_scale_f32_16x16x128_f8f6f4 v[122:125], v[172:179], v[192:199], v[122:125], v156, v155 op_sel_hi:[0,0,0]
	v_mfma_scale_f32_16x16x128_f8f6f4 v[110:113], v[164:171], v[200:207], v[110:113], v156, v155 op_sel_hi:[0,0,0]
	v_mfma_scale_f32_16x16x128_f8f6f4 v[106:109], v[172:179], v[200:207], v[106:109], v156, v155 op_sel_hi:[0,0,0]
	v_mfma_scale_f32_16x16x128_f8f6f4 v[94:97], v[164:171], v[208:215], v[94:97], v156, v155 op_sel_hi:[0,0,0]
	v_mfma_scale_f32_16x16x128_f8f6f4 v[90:93], v[172:179], v[208:215], v[90:93], v156, v155 op_sel_hi:[0,0,0]
	v_mfma_scale_f32_16x16x128_f8f6f4 v[78:81], v[164:171], v[216:223], v[78:81], v156, v155 op_sel_hi:[0,0,0]
	v_mfma_scale_f32_16x16x128_f8f6f4 v[74:77], v[172:179], v[216:223], v[74:77], v156, v155 op_sel_hi:[0,0,0]
	s_setprio 0
	s_setprio 1
	s_nop 0
	v_mfma_scale_f32_16x16x128_f8f6f4 v[118:121], v[180:187], v[192:199], v[118:121], v156, v155 op_sel_hi:[0,0,0]
	v_mfma_scale_f32_16x16x128_f8f6f4 v[114:117], v[224:231], v[192:199], v[114:117], v156, v155 op_sel_hi:[0,0,0]
	v_mfma_scale_f32_16x16x128_f8f6f4 v[102:105], v[180:187], v[200:207], v[102:105], v156, v155 op_sel_hi:[0,0,0]
	v_mfma_scale_f32_16x16x128_f8f6f4 v[98:101], v[224:231], v[200:207], v[98:101], v156, v155 op_sel_hi:[0,0,0]
	v_mfma_scale_f32_16x16x128_f8f6f4 v[86:89], v[180:187], v[208:215], v[86:89], v156, v155 op_sel_hi:[0,0,0]
	v_mfma_scale_f32_16x16x128_f8f6f4 v[82:85], v[224:231], v[208:215], v[82:85], v156, v155 op_sel_hi:[0,0,0]
	v_mfma_scale_f32_16x16x128_f8f6f4 v[70:73], v[180:187], v[216:223], v[70:73], v156, v155 op_sel_hi:[0,0,0]
	v_mfma_scale_f32_16x16x128_f8f6f4 v[66:69], v[224:231], v[216:223], v[66:69], v156, v155 op_sel_hi:[0,0,0]
	s_setprio 0
	s_barrier
	s_add_i32 s64, s53, s40
	v_lshl_add_u64 v[188:189], s[30:31], 0, v[132:133]
	s_mov_b32 m0, s64
	ds_read_b128 v[192:195], v154 offset:16384
	ds_read_b128 v[196:199], v154 offset:17408
	ds_read_b128 v[200:203], v154 offset:18432
	ds_read_b128 v[204:207], v154 offset:19456
	ds_read_b128 v[208:211], v154 offset:20480
	ds_read_b128 v[212:215], v154 offset:21504
	ds_read_b128 v[216:219], v154 offset:22528
	ds_read_b128 v[220:223], v154 offset:23552
	global_load_lds_dwordx4 v[188:189], off
	s_add_i32 m0, s64, 0x2000
	s_add_u32 s64, s30, 0x40000
	v_lshl_add_u64 v[190:191], s[30:31], 0, v[140:141]
	s_addc_u32 s65, s31, 0
	s_add_i32 s66, s54, s40
	global_load_lds_dwordx4 v[190:191], off
	v_lshl_add_u64 v[148:149], s[64:65], 0, v[132:133]
	s_mov_b32 m0, s66
	v_lshl_add_u64 v[232:233], s[34:35], 0, v[138:139]
	global_load_lds_dwordx4 v[148:149], off
	v_lshl_add_u64 v[148:149], s[64:65], 0, v[140:141]
	s_add_i32 m0, s66, 0x2000
	v_lshl_add_u64 v[234:235], s[34:35], 0, v[136:137]
	global_load_lds_dwordx4 v[148:149], off
	s_mov_b32 m0, s25
	s_nop 0
	global_load_lds_dwordx4 v[232:233], off
	s_mov_b32 m0, s44
	s_nop 0
	global_load_lds_dwordx4 v[234:235], off
	s_waitcnt vmcnt(8)
	s_waitcnt lgkmcnt(0)
	s_barrier
	s_setprio 1
	s_waitcnt lgkmcnt(0)
	s_nop 0
	v_mfma_scale_f32_16x16x128_f8f6f4 v[62:65], v[164:171], v[192:199], v[62:65], v156, v155 op_sel_hi:[0,0,0]
	v_mfma_scale_f32_16x16x128_f8f6f4 v[58:61], v[172:179], v[192:199], v[58:61], v156, v155 op_sel_hi:[0,0,0]
	v_mfma_scale_f32_16x16x128_f8f6f4 v[46:49], v[164:171], v[200:207], v[46:49], v156, v155 op_sel_hi:[0,0,0]
	v_mfma_scale_f32_16x16x128_f8f6f4 v[42:45], v[172:179], v[200:207], v[42:45], v156, v155 op_sel_hi:[0,0,0]
	v_mfma_scale_f32_16x16x128_f8f6f4 v[30:33], v[164:171], v[208:215], v[30:33], v156, v155 op_sel_hi:[0,0,0]
	v_mfma_scale_f32_16x16x128_f8f6f4 v[26:29], v[172:179], v[208:215], v[26:29], v156, v155 op_sel_hi:[0,0,0]
	v_mfma_scale_f32_16x16x128_f8f6f4 v[14:17], v[164:171], v[216:223], v[14:17], v156, v155 op_sel_hi:[0,0,0]
	v_mfma_scale_f32_16x16x128_f8f6f4 v[10:13], v[172:179], v[216:223], v[10:13], v156, v155 op_sel_hi:[0,0,0]
	s_setprio 0
	s_setprio 1
	s_nop 0
	v_mfma_scale_f32_16x16x128_f8f6f4 v[54:57], v[180:187], v[192:199], v[54:57], v156, v155 op_sel_hi:[0,0,0]
	v_mfma_scale_f32_16x16x128_f8f6f4 v[50:53], v[224:231], v[192:199], v[50:53], v156, v155 op_sel_hi:[0,0,0]
	v_mfma_scale_f32_16x16x128_f8f6f4 v[38:41], v[180:187], v[200:207], v[38:41], v156, v155 op_sel_hi:[0,0,0]
	v_mfma_scale_f32_16x16x128_f8f6f4 v[34:37], v[224:231], v[200:207], v[34:37], v156, v155 op_sel_hi:[0,0,0]
	v_mfma_scale_f32_16x16x128_f8f6f4 v[148:151], v[180:187], v[208:215], v[22:25], v156, v155 op_sel_hi:[0,0,0]
	v_mfma_scale_f32_16x16x128_f8f6f4 v[158:161], v[224:231], v[208:215], v[18:21], v156, v155 op_sel_hi:[0,0,0]
	v_mfma_scale_f32_16x16x128_f8f6f4 v[180:183], v[180:187], v[216:223], v[6:9], v156, v155 op_sel_hi:[0,0,0]
	v_mfma_scale_f32_16x16x128_f8f6f4 v[184:187], v[224:231], v[216:223], v[2:5], v156, v155 op_sel_hi:[0,0,0]
	s_setprio 0
	s_barrier
	s_add_i32 s64, 0, 0x18000
	s_add_i32 s65, 0, 0x1c000
	v_add_u32_e32 v22, s64, v135
	v_add_u32_e32 v162, s65, v135
	s_nop 0
	ds_read_b128 v[2:5], v22
	ds_read_b128 v[6:9], v22 offset:1024
	ds_read_b128 v[18:21], v22 offset:2048
	ds_read_b128 v[22:25], v22 offset:3072
	ds_read_b128 v[164:167], v162
	ds_read_b128 v[168:171], v162 offset:1024
	ds_read_b128 v[172:175], v162 offset:2048
	ds_read_b128 v[176:179], v162 offset:3072
	s_add_u32 s34, s34, 0x40000
	s_addc_u32 s35, s35, 0
	s_mov_b32 m0, s45
	v_lshl_add_u64 v[224:225], s[34:35], 0, v[138:139]
	ds_read_b128 v[192:195], v154 offset:32768
	ds_read_b128 v[196:199], v154 offset:33792
	ds_read_b128 v[200:203], v154 offset:34816
	ds_read_b128 v[204:207], v154 offset:35840
	ds_read_b128 v[208:211], v154 offset:36864
	ds_read_b128 v[212:215], v154 offset:37888
	ds_read_b128 v[216:219], v154 offset:38912
	ds_read_b128 v[220:223], v154 offset:39936
	global_load_lds_dwordx4 v[224:225], off
	v_lshl_add_u64 v[224:225], s[34:35], 0, v[136:137]
	s_mov_b32 m0, s48
	s_nop 0
	global_load_lds_dwordx4 v[224:225], off
	s_waitcnt vmcnt(8)
	s_waitcnt lgkmcnt(0)
	s_barrier
	s_setprio 1
	s_waitcnt lgkmcnt(0)
	s_nop 0
	v_mfma_scale_f32_16x16x128_f8f6f4 v[126:129], v[2:9], v[192:199], v[126:129], v156, v155 op_sel_hi:[0,0,0]
	v_mfma_scale_f32_16x16x128_f8f6f4 v[122:125], v[18:25], v[192:199], v[122:125], v156, v155 op_sel_hi:[0,0,0]
	v_mfma_scale_f32_16x16x128_f8f6f4 v[110:113], v[2:9], v[200:207], v[110:113], v156, v155 op_sel_hi:[0,0,0]
	v_mfma_scale_f32_16x16x128_f8f6f4 v[106:109], v[18:25], v[200:207], v[106:109], v156, v155 op_sel_hi:[0,0,0]
	v_mfma_scale_f32_16x16x128_f8f6f4 v[94:97], v[2:9], v[208:215], v[94:97], v156, v155 op_sel_hi:[0,0,0]
	v_mfma_scale_f32_16x16x128_f8f6f4 v[90:93], v[18:25], v[208:215], v[90:93], v156, v155 op_sel_hi:[0,0,0]
	v_mfma_scale_f32_16x16x128_f8f6f4 v[78:81], v[2:9], v[216:223], v[78:81], v156, v155 op_sel_hi:[0,0,0]
	v_mfma_scale_f32_16x16x128_f8f6f4 v[74:77], v[18:25], v[216:223], v[74:77], v156, v155 op_sel_hi:[0,0,0]
	s_setprio 0
	s_setprio 1
	s_nop 0
	v_mfma_scale_f32_16x16x128_f8f6f4 v[118:121], v[164:171], v[192:199], v[118:121], v156, v155 op_sel_hi:[0,0,0]
	v_mfma_scale_f32_16x16x128_f8f6f4 v[114:117], v[172:179], v[192:199], v[114:117], v156, v155 op_sel_hi:[0,0,0]
	v_mfma_scale_f32_16x16x128_f8f6f4 v[102:105], v[164:171], v[200:207], v[102:105], v156, v155 op_sel_hi:[0,0,0]
	v_mfma_scale_f32_16x16x128_f8f6f4 v[98:101], v[172:179], v[200:207], v[98:101], v156, v155 op_sel_hi:[0,0,0]
	v_mfma_scale_f32_16x16x128_f8f6f4 v[86:89], v[164:171], v[208:215], v[86:89], v156, v155 op_sel_hi:[0,0,0]
	v_mfma_scale_f32_16x16x128_f8f6f4 v[82:85], v[172:179], v[208:215], v[82:85], v156, v155 op_sel_hi:[0,0,0]
	v_mfma_scale_f32_16x16x128_f8f6f4 v[70:73], v[164:171], v[216:223], v[70:73], v156, v155 op_sel_hi:[0,0,0]
	v_mfma_scale_f32_16x16x128_f8f6f4 v[66:69], v[172:179], v[216:223], v[66:69], v156, v155 op_sel_hi:[0,0,0]
	s_setprio 0
	s_barrier
	s_add_i32 s34, s64, s40
	v_lshl_add_u64 v[188:189], v[188:189], 0, s[8:9]
	s_mov_b32 m0, s34
	ds_read_b128 v[192:195], v154 offset:49152
	ds_read_b128 v[196:199], v154 offset:50176
	ds_read_b128 v[200:203], v154 offset:51200
	ds_read_b128 v[204:207], v154 offset:52224
	ds_read_b128 v[208:211], v154 offset:53248
	ds_read_b128 v[212:215], v154 offset:54272
	ds_read_b128 v[216:219], v154 offset:55296
	ds_read_b128 v[220:223], v154 offset:56320
	global_load_lds_dwordx4 v[188:189], off
	s_add_i32 m0, s34, 0x2000
	s_add_u32 s30, s30, 0x40080
	v_lshl_add_u64 v[188:189], v[190:191], 0, s[8:9]
	s_addc_u32 s31, s31, 0
	s_add_i32 s34, s65, s40
	global_load_lds_dwordx4 v[188:189], off
	v_lshl_add_u64 v[188:189], s[30:31], 0, v[132:133]
	s_mov_b32 m0, s34
	s_nop 0
	global_load_lds_dwordx4 v[188:189], off
	v_lshl_add_u64 v[188:189], s[30:31], 0, v[140:141]
	s_add_i32 m0, s34, 0x2000
	s_nop 0
	global_load_lds_dwordx4 v[188:189], off
	v_lshl_add_u64 v[188:189], v[232:233], 0, s[8:9]
	s_mov_b32 m0, s50
	s_nop 0
	global_load_lds_dwordx4 v[188:189], off
	v_lshl_add_u64 v[188:189], v[234:235], 0, s[8:9]
	s_mov_b32 m0, s51
	s_nop 0
	global_load_lds_dwordx4 v[188:189], off
	s_waitcnt vmcnt(8)
	s_waitcnt lgkmcnt(0)
	s_barrier
	s_setprio 1
	s_waitcnt lgkmcnt(0)
	s_nop 0
	v_mfma_scale_f32_16x16x128_f8f6f4 v[62:65], v[2:9], v[192:199], v[62:65], v156, v155 op_sel_hi:[0,0,0]
	v_mfma_scale_f32_16x16x128_f8f6f4 v[58:61], v[18:25], v[192:199], v[58:61], v156, v155 op_sel_hi:[0,0,0]
	v_mfma_scale_f32_16x16x128_f8f6f4 v[46:49], v[2:9], v[200:207], v[46:49], v156, v155 op_sel_hi:[0,0,0]
	v_mfma_scale_f32_16x16x128_f8f6f4 v[42:45], v[18:25], v[200:207], v[42:45], v156, v155 op_sel_hi:[0,0,0]
	v_mfma_scale_f32_16x16x128_f8f6f4 v[30:33], v[2:9], v[208:215], v[30:33], v156, v155 op_sel_hi:[0,0,0]
	v_mfma_scale_f32_16x16x128_f8f6f4 v[26:29], v[18:25], v[208:215], v[26:29], v156, v155 op_sel_hi:[0,0,0]
	v_mfma_scale_f32_16x16x128_f8f6f4 v[14:17], v[2:9], v[216:223], v[14:17], v156, v155 op_sel_hi:[0,0,0]
	v_mfma_scale_f32_16x16x128_f8f6f4 v[10:13], v[18:25], v[216:223], v[10:13], v156, v155 op_sel_hi:[0,0,0]
	s_setprio 0
	s_setprio 1
	s_nop 0
	v_mfma_scale_f32_16x16x128_f8f6f4 v[54:57], v[164:171], v[192:199], v[54:57], v156, v155 op_sel_hi:[0,0,0]
	v_mfma_scale_f32_16x16x128_f8f6f4 v[50:53], v[172:179], v[192:199], v[50:53], v156, v155 op_sel_hi:[0,0,0]
	v_mfma_scale_f32_16x16x128_f8f6f4 v[38:41], v[164:171], v[200:207], v[38:41], v156, v155 op_sel_hi:[0,0,0]
	v_mfma_scale_f32_16x16x128_f8f6f4 v[34:37], v[172:179], v[200:207], v[34:37], v156, v155 op_sel_hi:[0,0,0]
	v_mfma_scale_f32_16x16x128_f8f6f4 v[22:25], v[164:171], v[208:215], v[148:151], v156, v155 op_sel_hi:[0,0,0]
	v_mfma_scale_f32_16x16x128_f8f6f4 v[18:21], v[172:179], v[208:215], v[158:161], v156, v155 op_sel_hi:[0,0,0]
	v_mfma_scale_f32_16x16x128_f8f6f4 v[6:9], v[164:171], v[216:223], v[180:183], v156, v155 op_sel_hi:[0,0,0]
	v_mfma_scale_f32_16x16x128_f8f6f4 v[2:5], v[172:179], v[216:223], v[184:187], v156, v155 op_sel_hi:[0,0,0]
	s_setprio 0
	s_barrier
	s_add_i32 s63, s63, 2
	s_add_u32 s26, s26, 0x100
	s_addc_u32 s27, s27, 0
	s_add_u32 s61, s61, 0x100
	s_addc_u32 s62, s62, 0
	s_cmp_gt_u32 s63, 13
	s_cbranch_scc0 .LBB0_1084
	s_and_b64 vcc, exec, s[10:11]
	s_cbranch_vccz .LBB0_1087
	s_nop 0
.LBB0_1087:
	v_pk_mul_f32 v[164:165], v[126:127], s[12:13] op_sel_hi:[1,0]
	v_pk_mul_f32 v[168:169], v[122:123], s[12:13] op_sel_hi:[1,0]
	v_exp_f32_e32 v164, v164
	v_exp_f32_e32 v165, v165
	v_exp_f32_e32 v168, v168
	v_exp_f32_e32 v169, v169
	v_pk_mul_f32 v[160:161], v[128:129], s[12:13] op_sel_hi:[1,0]
	v_pk_mul_f32 v[166:167], v[124:125], s[12:13] op_sel_hi:[1,0]
	v_pk_fma_f32 v[164:165], v[164:165], s[14:15], s[14:15] op_sel_hi:[1,0,0]
	v_exp_f32_e32 v160, v160
	v_exp_f32_e32 v161, v161
	v_exp_f32_e32 v166, v166
	v_exp_f32_e32 v167, v167
	v_rcp_f32_e32 v164, v164
	v_rcp_f32_e32 v165, v165
	v_pk_fma_f32 v[168:169], v[168:169], s[14:15], s[14:15] op_sel_hi:[1,0,0]
	v_pk_mul_f32 v[118:119], v[126:127], v[118:119]
	v_rcp_f32_e32 v168, v168
	v_rcp_f32_e32 v169, v169
	v_pk_fma_f32 v[160:161], v[160:161], s[14:15], s[14:15] op_sel_hi:[1,0,0]
	v_pk_fma_f32 v[166:167], v[166:167], s[14:15], s[14:15] op_sel_hi:[1,0,0]
	v_pk_mul_f32 v[118:119], v[118:119], v[164:165]
	v_pk_mul_f32 v[114:115], v[122:123], v[114:115]
	v_rcp_f32_e32 v160, v160
	v_rcp_f32_e32 v161, v161
	v_rcp_f32_e32 v166, v166
	v_rcp_f32_e32 v167, v167
	v_pk_mul_f32 v[114:115], v[114:115], v[168:169]
	v_med3_f32 v122, v118, s56, v157
	v_med3_f32 v119, v119, s56, v157
	v_mov_b32_e32 v118, 0
	v_cvt_pk_fp8_f32 v118, v122, v119
	v_med3_f32 v114, v114, s56, v157
	v_med3_f32 v115, v115, s56, v157
	v_mov_b32_e32 v119, 0
	v_cvt_pk_fp8_f32 v119, v114, v115
	v_pk_mul_f32 v[120:121], v[128:129], v[120:121]
	v_pk_mul_f32 v[116:117], v[124:125], v[116:117]
	v_pk_mul_f32 v[120:121], v[120:121], v[160:161]
	v_pk_mul_f32 v[116:117], v[116:117], v[166:167]
	v_med3_f32 v120, v120, s56, v157
	v_med3_f32 v121, v121, s56, v157
	v_med3_f32 v114, v116, s56, v157
	v_med3_f32 v115, v117, s56, v157
	v_pk_mul_f32 v[116:117], v[110:111], s[12:13] op_sel_hi:[1,0]
	v_cvt_pk_fp8_f32 v118, v120, v121 op_sel:[0,0,1]
	v_cvt_pk_fp8_f32 v119, v114, v115 op_sel:[0,0,1]
	v_exp_f32_e32 v116, v116
	v_exp_f32_e32 v117, v117
	v_pk_mul_f32 v[120:121], v[106:107], s[12:13] op_sel_hi:[1,0]
	v_lshl_add_u32 v158, s24, 8, v1
	v_lshl_or_b32 v148, s58, 7, v147
	v_mov_b64_e32 v[150:151], s[6:7]
	v_exp_f32_e32 v120, v120
	v_exp_f32_e32 v121, v121
	v_ashrrev_i32_e32 v149, 31, v148
	v_mad_i64_i32 v[114:115], s[26:27], v158, s55, v[150:151]
	v_lshl_add_u64 v[114:115], v[114:115], 0, v[148:149]
	global_store_dwordx2 v[114:115], v[118:119], off
	v_pk_mul_f32 v[114:115], v[112:113], s[12:13] op_sel_hi:[1,0]
	v_pk_mul_f32 v[118:119], v[108:109], s[12:13] op_sel_hi:[1,0]
	v_pk_fma_f32 v[116:117], v[116:117], s[14:15], s[14:15] op_sel_hi:[1,0,0]
	v_exp_f32_e32 v114, v114
	v_exp_f32_e32 v115, v115
	v_exp_f32_e32 v118, v118
	v_exp_f32_e32 v119, v119
	v_rcp_f32_e32 v116, v116
	v_rcp_f32_e32 v117, v117
	v_pk_fma_f32 v[120:121], v[120:121], s[14:15], s[14:15] op_sel_hi:[1,0,0]
	v_pk_mul_f32 v[102:103], v[110:111], v[102:103]
	v_rcp_f32_e32 v120, v120
	v_rcp_f32_e32 v121, v121
	v_pk_fma_f32 v[114:115], v[114:115], s[14:15], s[14:15] op_sel_hi:[1,0,0]
	v_pk_fma_f32 v[118:119], v[118:119], s[14:15], s[14:15] op_sel_hi:[1,0,0]
	v_pk_mul_f32 v[102:103], v[102:103], v[116:117]
	v_pk_mul_f32 v[98:99], v[106:107], v[98:99]
	v_rcp_f32_e32 v114, v114
	v_rcp_f32_e32 v115, v115
	v_rcp_f32_e32 v118, v118
	v_rcp_f32_e32 v119, v119
	v_pk_mul_f32 v[98:99], v[98:99], v[120:121]
	v_med3_f32 v106, v102, s56, v157
	v_med3_f32 v103, v103, s56, v157
	v_mov_b32_e32 v102, 0
	v_cvt_pk_fp8_f32 v102, v106, v103
	v_med3_f32 v98, v98, s56, v157
	v_med3_f32 v99, v99, s56, v157
	v_mov_b32_e32 v103, 0
	v_cvt_pk_fp8_f32 v103, v98, v99
	v_pk_mul_f32 v[104:105], v[112:113], v[104:105]
	v_pk_mul_f32 v[100:101], v[108:109], v[100:101]
	v_pk_mul_f32 v[104:105], v[104:105], v[114:115]
	v_pk_mul_f32 v[100:101], v[100:101], v[118:119]
	v_med3_f32 v104, v104, s56, v157
	v_med3_f32 v105, v105, s56, v157
	v_med3_f32 v98, v100, s56, v157
	v_med3_f32 v99, v101, s56, v157
	v_pk_mul_f32 v[100:101], v[94:95], s[12:13] op_sel_hi:[1,0]
	v_cvt_pk_fp8_f32 v102, v104, v105 op_sel:[0,0,1]
	v_cvt_pk_fp8_f32 v103, v98, v99 op_sel:[0,0,1]
	v_exp_f32_e32 v100, v100
	v_exp_f32_e32 v101, v101
	v_pk_mul_f32 v[104:105], v[90:91], s[12:13] op_sel_hi:[1,0]
	v_or_b32_e32 v122, 16, v158
	v_exp_f32_e32 v104, v104
	v_exp_f32_e32 v105, v105
	v_mad_i64_i32 v[98:99], s[26:27], v122, s55, v[150:151]
	v_lshl_add_u64 v[98:99], v[98:99], 0, v[148:149]
	global_store_dwordx2 v[98:99], v[102:103], off
	v_pk_mul_f32 v[98:99], v[96:97], s[12:13] op_sel_hi:[1,0]
	v_pk_mul_f32 v[102:103], v[92:93], s[12:13] op_sel_hi:[1,0]
	v_pk_fma_f32 v[100:101], v[100:101], s[14:15], s[14:15] op_sel_hi:[1,0,0]
	v_exp_f32_e32 v98, v98
	v_exp_f32_e32 v99, v99
	v_exp_f32_e32 v102, v102
	v_exp_f32_e32 v103, v103
	v_rcp_f32_e32 v100, v100
	v_rcp_f32_e32 v101, v101
	v_pk_fma_f32 v[104:105], v[104:105], s[14:15], s[14:15] op_sel_hi:[1,0,0]
	v_pk_mul_f32 v[86:87], v[94:95], v[86:87]
	v_rcp_f32_e32 v104, v104
	v_rcp_f32_e32 v105, v105
	v_pk_fma_f32 v[98:99], v[98:99], s[14:15], s[14:15] op_sel_hi:[1,0,0]
	v_pk_fma_f32 v[102:103], v[102:103], s[14:15], s[14:15] op_sel_hi:[1,0,0]
	v_pk_mul_f32 v[86:87], v[86:87], v[100:101]
	v_pk_mul_f32 v[82:83], v[90:91], v[82:83]
	v_rcp_f32_e32 v98, v98
	v_rcp_f32_e32 v99, v99
	v_rcp_f32_e32 v102, v102
	v_rcp_f32_e32 v103, v103
	v_pk_mul_f32 v[82:83], v[82:83], v[104:105]
	v_med3_f32 v90, v86, s56, v157
	v_med3_f32 v87, v87, s56, v157
	v_mov_b32_e32 v86, 0
	v_cvt_pk_fp8_f32 v86, v90, v87
	v_med3_f32 v82, v82, s56, v157
	v_med3_f32 v83, v83, s56, v157
	v_mov_b32_e32 v87, 0
	v_cvt_pk_fp8_f32 v87, v82, v83
	v_pk_mul_f32 v[88:89], v[96:97], v[88:89]
	v_pk_mul_f32 v[84:85], v[92:93], v[84:85]
	v_pk_mul_f32 v[88:89], v[88:89], v[98:99]
	v_pk_mul_f32 v[84:85], v[84:85], v[102:103]
	v_med3_f32 v88, v88, s56, v157
	v_med3_f32 v89, v89, s56, v157
	v_med3_f32 v82, v84, s56, v157
	v_med3_f32 v83, v85, s56, v157
	v_pk_mul_f32 v[84:85], v[78:79], s[12:13] op_sel_hi:[1,0]
	v_cvt_pk_fp8_f32 v86, v88, v89 op_sel:[0,0,1]
	v_cvt_pk_fp8_f32 v87, v82, v83 op_sel:[0,0,1]
	v_exp_f32_e32 v84, v84
	v_exp_f32_e32 v85, v85
	v_pk_mul_f32 v[88:89], v[74:75], s[12:13] op_sel_hi:[1,0]
	v_or_b32_e32 v106, 32, v158
	v_exp_f32_e32 v88, v88
	v_exp_f32_e32 v89, v89
	v_mad_i64_i32 v[82:83], s[26:27], v106, s55, v[150:151]
	v_lshl_add_u64 v[82:83], v[82:83], 0, v[148:149]
	global_store_dwordx2 v[82:83], v[86:87], off
	v_pk_mul_f32 v[82:83], v[80:81], s[12:13] op_sel_hi:[1,0]
	v_pk_mul_f32 v[86:87], v[76:77], s[12:13] op_sel_hi:[1,0]
	v_pk_fma_f32 v[84:85], v[84:85], s[14:15], s[14:15] op_sel_hi:[1,0,0]
	v_exp_f32_e32 v82, v82
	v_exp_f32_e32 v83, v83
	v_exp_f32_e32 v86, v86
	v_exp_f32_e32 v87, v87
	v_rcp_f32_e32 v84, v84
	v_rcp_f32_e32 v85, v85
	v_pk_fma_f32 v[88:89], v[88:89], s[14:15], s[14:15] op_sel_hi:[1,0,0]
	v_pk_mul_f32 v[70:71], v[78:79], v[70:71]
	v_rcp_f32_e32 v88, v88
	v_rcp_f32_e32 v89, v89
	v_pk_fma_f32 v[82:83], v[82:83], s[14:15], s[14:15] op_sel_hi:[1,0,0]
	v_pk_fma_f32 v[86:87], v[86:87], s[14:15], s[14:15] op_sel_hi:[1,0,0]
	v_pk_mul_f32 v[70:71], v[70:71], v[84:85]
	v_pk_mul_f32 v[66:67], v[74:75], v[66:67]
	v_rcp_f32_e32 v82, v82
	v_rcp_f32_e32 v83, v83
	v_rcp_f32_e32 v86, v86
	v_rcp_f32_e32 v87, v87
	v_pk_mul_f32 v[66:67], v[66:67], v[88:89]
	v_med3_f32 v74, v70, s56, v157
	v_med3_f32 v71, v71, s56, v157
	v_mov_b32_e32 v70, 0
	v_cvt_pk_fp8_f32 v70, v74, v71
	v_med3_f32 v66, v66, s56, v157
	v_med3_f32 v67, v67, s56, v157
	v_mov_b32_e32 v71, 0
	v_cvt_pk_fp8_f32 v71, v66, v67
	v_pk_mul_f32 v[72:73], v[80:81], v[72:73]
	v_pk_mul_f32 v[68:69], v[76:77], v[68:69]
	v_pk_mul_f32 v[72:73], v[72:73], v[82:83]
	v_pk_mul_f32 v[68:69], v[68:69], v[86:87]
	v_med3_f32 v72, v72, s56, v157
	v_med3_f32 v73, v73, s56, v157
	v_med3_f32 v66, v68, s56, v157
	v_med3_f32 v67, v69, s56, v157
	v_pk_mul_f32 v[68:69], v[62:63], s[12:13] op_sel_hi:[1,0]
	v_cvt_pk_fp8_f32 v70, v72, v73 op_sel:[0,0,1]
	v_cvt_pk_fp8_f32 v71, v66, v67 op_sel:[0,0,1]
	v_exp_f32_e32 v68, v68
	v_exp_f32_e32 v69, v69
	v_pk_mul_f32 v[72:73], v[58:59], s[12:13] op_sel_hi:[1,0]
	v_or_b32_e32 v90, 48, v158
	v_exp_f32_e32 v72, v72
	v_exp_f32_e32 v73, v73
	v_mad_i64_i32 v[66:67], s[26:27], v90, s55, v[150:151]
	v_lshl_add_u64 v[66:67], v[66:67], 0, v[148:149]
	global_store_dwordx2 v[66:67], v[70:71], off
	v_pk_mul_f32 v[66:67], v[64:65], s[12:13] op_sel_hi:[1,0]
	v_pk_mul_f32 v[70:71], v[60:61], s[12:13] op_sel_hi:[1,0]
	v_pk_fma_f32 v[68:69], v[68:69], s[14:15], s[14:15] op_sel_hi:[1,0,0]
	v_exp_f32_e32 v66, v66
	v_exp_f32_e32 v67, v67
	v_exp_f32_e32 v70, v70
	v_exp_f32_e32 v71, v71
	v_rcp_f32_e32 v68, v68
	v_rcp_f32_e32 v69, v69
	v_pk_fma_f32 v[72:73], v[72:73], s[14:15], s[14:15] op_sel_hi:[1,0,0]
	v_pk_mul_f32 v[54:55], v[62:63], v[54:55]
	v_rcp_f32_e32 v72, v72
	v_rcp_f32_e32 v73, v73
	v_pk_fma_f32 v[66:67], v[66:67], s[14:15], s[14:15] op_sel_hi:[1,0,0]
	v_pk_fma_f32 v[70:71], v[70:71], s[14:15], s[14:15] op_sel_hi:[1,0,0]
	v_pk_mul_f32 v[54:55], v[54:55], v[68:69]
	v_pk_mul_f32 v[50:51], v[58:59], v[50:51]
	v_rcp_f32_e32 v66, v66
	v_rcp_f32_e32 v67, v67
	v_rcp_f32_e32 v70, v70
	v_rcp_f32_e32 v71, v71
	v_pk_mul_f32 v[50:51], v[50:51], v[72:73]
	v_med3_f32 v58, v54, s56, v157
	v_med3_f32 v55, v55, s56, v157
	v_mov_b32_e32 v54, 0
	v_cvt_pk_fp8_f32 v54, v58, v55
	v_med3_f32 v50, v50, s56, v157
	v_med3_f32 v51, v51, s56, v157
	v_mov_b32_e32 v55, 0
	v_cvt_pk_fp8_f32 v55, v50, v51
	v_pk_mul_f32 v[56:57], v[64:65], v[56:57]
	v_pk_mul_f32 v[52:53], v[60:61], v[52:53]
	v_pk_mul_f32 v[56:57], v[56:57], v[66:67]
	v_pk_mul_f32 v[52:53], v[52:53], v[70:71]
	v_med3_f32 v56, v56, s56, v157
	v_med3_f32 v57, v57, s56, v157
	v_med3_f32 v50, v52, s56, v157
	v_med3_f32 v51, v53, s56, v157
	v_pk_mul_f32 v[52:53], v[46:47], s[12:13] op_sel_hi:[1,0]
	v_cvt_pk_fp8_f32 v54, v56, v57 op_sel:[0,0,1]
	v_cvt_pk_fp8_f32 v55, v50, v51 op_sel:[0,0,1]
	v_exp_f32_e32 v52, v52
	v_exp_f32_e32 v53, v53
	v_pk_mul_f32 v[56:57], v[42:43], s[12:13] op_sel_hi:[1,0]
	v_add_u32_e32 v74, 0x80, v158
	v_exp_f32_e32 v56, v56
	v_exp_f32_e32 v57, v57
	v_mad_i64_i32 v[50:51], s[26:27], v74, s55, v[150:151]
	v_lshl_add_u64 v[50:51], v[50:51], 0, v[148:149]
	global_store_dwordx2 v[50:51], v[54:55], off
	v_pk_mul_f32 v[50:51], v[48:49], s[12:13] op_sel_hi:[1,0]
	v_pk_mul_f32 v[54:55], v[44:45], s[12:13] op_sel_hi:[1,0]
	v_pk_fma_f32 v[52:53], v[52:53], s[14:15], s[14:15] op_sel_hi:[1,0,0]
	v_exp_f32_e32 v50, v50
	v_exp_f32_e32 v51, v51
	v_exp_f32_e32 v54, v54
	v_exp_f32_e32 v55, v55
	v_rcp_f32_e32 v52, v52
	v_rcp_f32_e32 v53, v53
	v_pk_fma_f32 v[56:57], v[56:57], s[14:15], s[14:15] op_sel_hi:[1,0,0]
	v_pk_mul_f32 v[38:39], v[46:47], v[38:39]
	v_rcp_f32_e32 v56, v56
	v_rcp_f32_e32 v57, v57
	v_pk_fma_f32 v[50:51], v[50:51], s[14:15], s[14:15] op_sel_hi:[1,0,0]
	v_pk_fma_f32 v[54:55], v[54:55], s[14:15], s[14:15] op_sel_hi:[1,0,0]
	v_pk_mul_f32 v[38:39], v[38:39], v[52:53]
	v_pk_mul_f32 v[34:35], v[42:43], v[34:35]
	v_rcp_f32_e32 v50, v50
	v_rcp_f32_e32 v51, v51
	v_rcp_f32_e32 v54, v54
	v_rcp_f32_e32 v55, v55
	v_pk_mul_f32 v[34:35], v[34:35], v[56:57]
	v_med3_f32 v42, v38, s56, v157
	v_med3_f32 v39, v39, s56, v157
	v_mov_b32_e32 v38, 0
	v_cvt_pk_fp8_f32 v38, v42, v39
	v_med3_f32 v34, v34, s56, v157
	v_med3_f32 v35, v35, s56, v157
	v_mov_b32_e32 v39, 0
	v_cvt_pk_fp8_f32 v39, v34, v35
	v_pk_mul_f32 v[40:41], v[48:49], v[40:41]
	v_pk_mul_f32 v[36:37], v[44:45], v[36:37]
	v_pk_mul_f32 v[40:41], v[40:41], v[50:51]
	v_pk_mul_f32 v[36:37], v[36:37], v[54:55]
	v_med3_f32 v40, v40, s56, v157
	v_med3_f32 v41, v41, s56, v157
	v_med3_f32 v34, v36, s56, v157
	v_med3_f32 v35, v37, s56, v157
	v_pk_mul_f32 v[36:37], v[30:31], s[12:13] op_sel_hi:[1,0]
	v_cvt_pk_fp8_f32 v38, v40, v41 op_sel:[0,0,1]
	v_cvt_pk_fp8_f32 v39, v34, v35 op_sel:[0,0,1]
	v_exp_f32_e32 v36, v36
	v_exp_f32_e32 v37, v37
	v_pk_mul_f32 v[40:41], v[26:27], s[12:13] op_sel_hi:[1,0]
	v_add_u32_e32 v58, 0x90, v158
	v_exp_f32_e32 v40, v40
	v_exp_f32_e32 v41, v41
	v_mad_i64_i32 v[34:35], s[26:27], v58, s55, v[150:151]
	v_lshl_add_u64 v[34:35], v[34:35], 0, v[148:149]
	global_store_dwordx2 v[34:35], v[38:39], off
	v_pk_mul_f32 v[34:35], v[32:33], s[12:13] op_sel_hi:[1,0]
	v_pk_mul_f32 v[38:39], v[28:29], s[12:13] op_sel_hi:[1,0]
	v_pk_fma_f32 v[36:37], v[36:37], s[14:15], s[14:15] op_sel_hi:[1,0,0]
	v_exp_f32_e32 v34, v34
	v_exp_f32_e32 v35, v35
	v_exp_f32_e32 v38, v38
	v_exp_f32_e32 v39, v39
	v_rcp_f32_e32 v36, v36
	v_rcp_f32_e32 v37, v37
	v_pk_fma_f32 v[40:41], v[40:41], s[14:15], s[14:15] op_sel_hi:[1,0,0]
	v_pk_mul_f32 v[22:23], v[30:31], v[22:23]
	v_rcp_f32_e32 v40, v40
	v_rcp_f32_e32 v41, v41
	v_pk_fma_f32 v[34:35], v[34:35], s[14:15], s[14:15] op_sel_hi:[1,0,0]
	v_pk_fma_f32 v[38:39], v[38:39], s[14:15], s[14:15] op_sel_hi:[1,0,0]
	v_pk_mul_f32 v[22:23], v[22:23], v[36:37]
	v_pk_mul_f32 v[18:19], v[26:27], v[18:19]
	v_rcp_f32_e32 v34, v34
	v_rcp_f32_e32 v35, v35
	v_rcp_f32_e32 v38, v38
	v_rcp_f32_e32 v39, v39
	v_pk_mul_f32 v[18:19], v[18:19], v[40:41]
	v_med3_f32 v26, v22, s56, v157
	v_med3_f32 v23, v23, s56, v157
	v_mov_b32_e32 v22, 0
	v_cvt_pk_fp8_f32 v22, v26, v23
	v_med3_f32 v18, v18, s56, v157
	v_med3_f32 v19, v19, s56, v157
	v_mov_b32_e32 v23, 0
	v_cvt_pk_fp8_f32 v23, v18, v19
	v_pk_mul_f32 v[24:25], v[32:33], v[24:25]
	v_pk_mul_f32 v[20:21], v[28:29], v[20:21]
	v_pk_mul_f32 v[24:25], v[24:25], v[34:35]
	v_pk_mul_f32 v[20:21], v[20:21], v[38:39]
	v_med3_f32 v24, v24, s56, v157
	v_med3_f32 v25, v25, s56, v157
	v_med3_f32 v18, v20, s56, v157
	v_med3_f32 v19, v21, s56, v157
	v_pk_mul_f32 v[20:21], v[14:15], s[12:13] op_sel_hi:[1,0]
	v_cvt_pk_fp8_f32 v22, v24, v25 op_sel:[0,0,1]
	v_cvt_pk_fp8_f32 v23, v18, v19 op_sel:[0,0,1]
	v_exp_f32_e32 v20, v20
	v_exp_f32_e32 v21, v21
	v_pk_mul_f32 v[24:25], v[10:11], s[12:13] op_sel_hi:[1,0]
	v_add_u32_e32 v42, 0xa0, v158
	v_exp_f32_e32 v24, v24
	v_exp_f32_e32 v25, v25
	v_mad_i64_i32 v[18:19], s[26:27], v42, s55, v[150:151]
	v_lshl_add_u64 v[18:19], v[18:19], 0, v[148:149]
	global_store_dwordx2 v[18:19], v[22:23], off
	v_pk_mul_f32 v[18:19], v[16:17], s[12:13] op_sel_hi:[1,0]
	v_pk_mul_f32 v[22:23], v[12:13], s[12:13] op_sel_hi:[1,0]
	v_pk_fma_f32 v[20:21], v[20:21], s[14:15], s[14:15] op_sel_hi:[1,0,0]
	v_exp_f32_e32 v18, v18
	v_exp_f32_e32 v19, v19
	v_exp_f32_e32 v22, v22
	v_exp_f32_e32 v23, v23
	v_rcp_f32_e32 v20, v20
	v_rcp_f32_e32 v21, v21
	v_pk_fma_f32 v[24:25], v[24:25], s[14:15], s[14:15] op_sel_hi:[1,0,0]
	v_pk_mul_f32 v[6:7], v[14:15], v[6:7]
	v_rcp_f32_e32 v24, v24
	v_rcp_f32_e32 v25, v25
	v_pk_fma_f32 v[18:19], v[18:19], s[14:15], s[14:15] op_sel_hi:[1,0,0]
	v_pk_fma_f32 v[22:23], v[22:23], s[14:15], s[14:15] op_sel_hi:[1,0,0]
	v_pk_mul_f32 v[6:7], v[6:7], v[20:21]
	v_pk_mul_f32 v[2:3], v[10:11], v[2:3]
	v_rcp_f32_e32 v18, v18
	v_rcp_f32_e32 v19, v19
	v_rcp_f32_e32 v22, v22
	v_rcp_f32_e32 v23, v23
	v_pk_mul_f32 v[2:3], v[2:3], v[24:25]
	v_med3_f32 v10, v6, s56, v157
	v_med3_f32 v7, v7, s56, v157
	v_mov_b32_e32 v6, 0
	v_cvt_pk_fp8_f32 v6, v10, v7
	v_med3_f32 v2, v2, s56, v157
	v_med3_f32 v3, v3, s56, v157
	v_mov_b32_e32 v7, 0
	v_cvt_pk_fp8_f32 v7, v2, v3
	v_pk_mul_f32 v[8:9], v[16:17], v[8:9]
	v_pk_mul_f32 v[4:5], v[12:13], v[4:5]
	v_pk_mul_f32 v[8:9], v[8:9], v[18:19]
	v_pk_mul_f32 v[4:5], v[4:5], v[22:23]
	v_med3_f32 v8, v8, s56, v157
	v_med3_f32 v9, v9, s56, v157
	v_med3_f32 v2, v4, s56, v157
	v_med3_f32 v3, v5, s56, v157
	v_cvt_pk_fp8_f32 v6, v8, v9 op_sel:[0,0,1]
	v_cvt_pk_fp8_f32 v7, v2, v3 op_sel:[0,0,1]
	v_add_u32_e32 v26, 0xb0, v158
	v_mad_i64_i32 v[2:3], s[26:27], v26, s55, v[150:151]
	v_lshl_add_u64 v[2:3], v[2:3], 0, v[148:149]
	s_andn2_b64 vcc, exec, s[2:3]
	s_mov_b64 s[2:3], -1
	global_store_dwordx2 v[2:3], v[6:7], off
	s_cbranch_vccnz .LBB0_1078
	s_andn2_b64 vcc, exec, s[4:5]
	s_cbranch_vccnz .LBB0_1077
	s_nop 0
	s_branch .LBB0_1077
.LBB0_1090:
	s_waitcnt vmcnt(0)
	v_readlane_b32 s44, v242, 8
	v_readlane_b32 s45, v242, 9
	s_and_b64 vcc, exec, s[10:11]
	s_cbranch_vccz .Lp14_noalign
	s_barrier
.Lp14_noalign:
	s_barrier
